# v32 + at_dil QK step: bias-table LDS reads hoisted into the MFMA ladder (fresh registers), waits regenerated
# baseline (speedup 1.0000x reference)
; #define LAS __attribute__((address_space(3)))
; __device__ __forceinline__ int crow(int r, int hi) { return (r & 3) + 8 * (r >> 2) + 4 * hi; }
; __device__ __forceinline__ unsigned cvtpk(float lo, float hi) { f32x2_t v = {lo, hi}; bf16x2_t b = __builtin_convertvector(v, bf16x2_t); return __builtin_bit_cast(unsigned, b); }
; __device__ __forceinline__ void qkt(f32x16& p0, f32x16& p1, const LAS unsigned char* Kb, const bf16x8 (&qr)[4], float cinit, int r32, int hi) {
;     const int sw = (r32 >> 1) & 7;
;     bf16x8 kf[8];
; #pragma unroll
;     for (int d0 = 0; d0 < 4; ++d0) {
;         unsigned ka = (unsigned)(uintptr_t)Kb + r32 * 128 + (((2 * d0 + hi) ^ sw) << 4); asm volatile("" : "+v"(ka));
;         kf[2 * d0] = *(const LAS bf16x8*)(uintptr_t)ka;
;         kf[2 * d0 + 1] = *(const LAS bf16x8*)(uintptr_t)(ka + 4096);
;     }
; #pragma unroll
;     for (int r = 0; r < 16; ++r) { p0[r] = cinit; p1[r] = cinit; }
;     __builtin_amdgcn_sched_barrier(0);
; #pragma unroll
;     for (int d0 = 0; d0 < 4; ++d0) {
;         p0 = __builtin_amdgcn_mfma_f32_32x32x16_bf16(kf[2 * d0], qr[d0], p0, 0, 0, 0);
;         p1 = __builtin_amdgcn_mfma_f32_32x32x16_bf16(kf[2 * d0 + 1], qr[d0], p1, 0, 0, 0);
;     }
; __device__ __forceinline__ void at_dil(const Args& a, LAS unsigned char* lds, int layer) {
;     ...
;                 if (tt >= tt_lo) {
;                     f32x16 p0, p1;
;                     qkt(p0, p1, lds + L_K + tt * 8192, qr, -m_dil, r32, hi);
;                     const LAS float* tb = tab + (32 * wid + r32 + 192 - 64 * tt - 4 * hi - 63);
; #pragma unroll
;                     for (int r = 0; r < 16; ++r) { p0[r] += tb[63 - crow(r, 0)]; p1[r] += tb[31 - crow(r, 0)]; }
;                     exp_sum(p0, p1, l_part);
;                     pw[j][0] = (u32x4){cvtpk(p0[0], p0[1]), cvtpk(p0[2], p0[3]), cvtpk(p0[4], p0[5]), cvtpk(p0[6], p0[7])};
;                     pw[j][1] = (u32x4){cvtpk(p0[8], p0[9]), cvtpk(p0[10], p0[11]), cvtpk(p0[12], p0[13]), cvtpk(p0[14], p0[15])};
;                     pw[j][2] = (u32x4){cvtpk(p1[0], p1[1]), cvtpk(p1[2], p1[3]), cvtpk(p1[4], p1[5]), cvtpk(p1[6], p1[7])};
;                     pw[j][3] = (u32x4){cvtpk(p1[8], p1[9]), cvtpk(p1[10], p1[11]), cvtpk(p1[12], p1[13]), cvtpk(p1[14], p1[15])};
.LBB0_563:
	v_mov_b32_e32 v138, 0
	s_cmp_lt_i32 s42, s54
	v_lshlrev_b32_e32 v52, 2, v139
	s_cbranch_scc1 .LBB0_572
	s_nop 4
	v_add_u32_e32 v18, s46, v143
	v_add_u32_e32 v19, v144, v18
	ds_read_b128 v[36:39], v19
	ds_read_b128 v[54:57], v19 offset:4096
	v_add_u32_e32 v19, v142, v18
	ds_read_b128 v[58:61], v19
	ds_read_b128 v[62:65], v19 offset:4096
	v_add_u32_e32 v19, v141, v18
	v_add_u32_e32 v18, v140, v18
	ds_read_b128 v[88:91], v19
	ds_read_b128 v[96:99], v19 offset:4096
	ds_read_b128 v[104:107], v18
	ds_read_b128 v[112:115], v18 offset:4096
	s_waitcnt lgkmcnt(7)
	v_mfma_f32_32x32x16_bf16 v[18:33], v[36:39], v[68:71], v[2:17]
	v_add_lshl_u32 v53, v136, s43, 2
	v_add3_u32 v53, s73, v52, v53
	s_waitcnt lgkmcnt(6)
	v_mfma_f32_32x32x16_bf16 v[36:51], v[54:57], v[68:71], v[2:17]
	ds_read2_b32 v[162:163], v53 offset0:191 offset1:192
	ds_read2_b32 v[164:165], v53 offset0:189 offset1:190
	ds_read2_b32 v[166:167], v53 offset0:159 offset1:160
	ds_read2_b32 v[168:169], v53 offset0:157 offset1:158
	s_waitcnt lgkmcnt(9)
	v_mfma_f32_32x32x16_bf16 v[18:33], v[58:61], v[72:75], v[18:33]
	ds_read2_b32 v[170:171], v53 offset0:183 offset1:184
	ds_read2_b32 v[172:173], v53 offset0:181 offset1:182
	s_waitcnt lgkmcnt(10)
	v_mfma_f32_32x32x16_bf16 v[36:51], v[62:65], v[72:75], v[36:51]
	ds_read2_b32 v[174:175], v53 offset0:151 offset1:152
	ds_read2_b32 v[176:177], v53 offset0:149 offset1:150
	s_waitcnt lgkmcnt(11)
	v_mfma_f32_32x32x16_bf16 v[18:33], v[88:91], v[76:79], v[18:33]
	ds_read2_b32 v[178:179], v53 offset0:175 offset1:176
	ds_read2_b32 v[180:181], v53 offset0:173 offset1:174
	s_waitcnt lgkmcnt(12)
	v_mfma_f32_32x32x16_bf16 v[36:51], v[96:99], v[76:79], v[36:51]
	ds_read2_b32 v[182:183], v53 offset0:143 offset1:144
	ds_read2_b32 v[184:185], v53 offset0:141 offset1:142
	s_waitcnt lgkmcnt(13)
	v_mfma_f32_32x32x16_bf16 v[18:33], v[104:107], v[80:83], v[18:33]
	ds_read2_b32 v[186:187], v53 offset0:167 offset1:168
	s_waitcnt lgkmcnt(12)
	ds_read2_b32 v[188:189], v53 offset0:135 offset1:136
	v_mfma_f32_32x32x16_bf16 v[36:51], v[112:115], v[80:83], v[36:51]
	ds_read2_b32 v[190:191], v53 offset0:165 offset1:166
	s_waitcnt lgkmcnt(12)
	ds_read2_b32 v[192:193], v53 offset0:133 offset1:134
	s_nop 11
	v_add_f32_e32 v55, v18, v163
	v_add_f32_e32 v54, v19, v162
	v_add_f32_e32 v57, v20, v165
	v_add_f32_e32 v56, v21, v164
	v_exp_f32_e32 v55, v55
	v_add_f32_e32 v59, v36, v167
	v_add_f32_e32 v58, v37, v166
	s_waitcnt lgkmcnt(12)
	v_add_f32_e32 v61, v38, v169
	v_add_f32_e32 v60, v39, v168
	s_waitcnt lgkmcnt(11)
	v_add_f32_e32 v62, v22, v171
	s_waitcnt lgkmcnt(9)
	v_add_f32_e32 v37, v40, v175
	v_add_f32_e32 v40, v23, v170
	v_add_f32_e32 v36, v41, v174
	v_add_f32_e32 v41, v24, v173
	s_waitcnt lgkmcnt(8)
	v_add_f32_e32 v39, v42, v177
	v_add_f32_e32 v42, v25, v172
	v_add_f32_e32 v38, v43, v176
	s_waitcnt lgkmcnt(7)
	v_add_f32_e32 v43, v26, v179
	v_add_f32_e32 v63, v27, v178
	s_waitcnt lgkmcnt(5)
	v_add_f32_e32 v44, v44, v183
	v_add_f32_e32 v45, v45, v182
	v_add_f32_e32 v64, v28, v181
	v_add_f32_e32 v65, v29, v180
	v_exp_f32_e32 v59, v59
	s_waitcnt lgkmcnt(4)
	v_add_f32_e32 v46, v46, v185
	v_add_f32_e32 v47, v47, v184
	s_waitcnt lgkmcnt(3)
	v_add_f32_e32 v66, v30, v187
	s_waitcnt lgkmcnt(2)
	v_add_f32_e32 v48, v48, v189
	v_exp_f32_e32 v19, v54
	v_exp_f32_e32 v21, v58
	v_add_f32_e32 v53, v31, v186
	v_add_f32_e32 v49, v49, v188
	v_add_f32_e32 v18, v55, v59
	v_mov_b32_e32 v20, v35
	s_waitcnt lgkmcnt(1)
	v_add_f32_e32 v67, v32, v191
	v_add_f32_e32 v88, v33, v190
	v_exp_f32_e32 v54, v57
	v_exp_f32_e32 v57, v61
	v_pk_add_f32 v[22:23], v[18:19], v[20:21]
	v_exp_f32_e32 v18, v56
	s_waitcnt lgkmcnt(0)
	v_add_f32_e32 v50, v50, v25
	v_exp_f32_e32 v25, v60
	v_pk_add_f32 v[22:23], v[22:23], v[22:23] op_sel:[0,1] op_sel_hi:[1,0]
	v_add_f32_e32 v51, v51, v24
	v_add_f32_e32 v24, v54, v57
	v_mov_b32_e32 v23, v18
	v_exp_f32_e32 v20, v62
	v_exp_f32_e32 v56, v37
	v_pk_add_f32 v[22:23], v[22:23], v[24:25]
	v_exp_f32_e32 v24, v40
	v_exp_f32_e32 v27, v36
	v_pk_add_f32 v[22:23], v[22:23], v[22:23] op_sel:[0,1] op_sel_hi:[1,0]
	v_add_f32_e32 v26, v20, v56
	v_mov_b32_e32 v23, v24
	v_exp_f32_e32 v40, v41
	v_exp_f32_e32 v41, v39
	v_pk_add_f32 v[22:23], v[22:23], v[26:27]
	v_exp_f32_e32 v26, v42
	v_exp_f32_e32 v29, v38
	v_pk_add_f32 v[22:23], v[22:23], v[22:23] op_sel:[0,1] op_sel_hi:[1,0]
	v_add_f32_e32 v28, v40, v41
	v_mov_b32_e32 v23, v26
	v_exp_f32_e32 v42, v43
	v_exp_f32_e32 v43, v44
	v_pk_add_f32 v[22:23], v[22:23], v[28:29]
	v_exp_f32_e32 v28, v63
	v_exp_f32_e32 v31, v45
	v_pk_add_f32 v[22:23], v[22:23], v[22:23] op_sel:[0,1] op_sel_hi:[1,0]
	v_add_f32_e32 v30, v42, v43
	v_mov_b32_e32 v23, v28
	v_exp_f32_e32 v44, v64
	v_exp_f32_e32 v45, v46
	v_pk_add_f32 v[22:23], v[22:23], v[30:31]
	v_exp_f32_e32 v30, v65
	v_exp_f32_e32 v33, v47
	v_pk_add_f32 v[22:23], v[22:23], v[22:23] op_sel:[0,1] op_sel_hi:[1,0]
	v_add_f32_e32 v32, v44, v45
	v_mov_b32_e32 v23, v30
	v_exp_f32_e32 v46, v66
	v_exp_f32_e32 v47, v48
	v_pk_add_f32 v[22:23], v[22:23], v[32:33]
	v_exp_f32_e32 v32, v53
	v_exp_f32_e32 v37, v49
	v_pk_add_f32 v[22:23], v[22:23], v[22:23] op_sel:[0,1] op_sel_hi:[1,0]
	v_add_f32_e32 v36, v46, v47
	v_mov_b32_e32 v23, v32
	v_exp_f32_e32 v48, v67
	v_exp_f32_e32 v49, v50
	v_pk_add_f32 v[22:23], v[22:23], v[36:37]
	v_exp_f32_e32 v36, v88
	v_exp_f32_e32 v39, v51
	v_pk_add_f32 v[22:23], v[22:23], v[22:23] op_sel:[0,1] op_sel_hi:[1,0]
	v_add_f32_e32 v38, v48, v49
	v_mov_b32_e32 v23, v36
	v_pk_add_f32 v[22:23], v[22:23], v[38:39]
	v_cvt_pk_bf16_f32 v88, v55, v19
	v_add_f32_e32 v22, v22, v23
	v_add_f32_e32 v138, 0, v22
	v_cvt_pk_bf16_f32 v89, v54, v18
	v_cvt_pk_bf16_f32 v90, v20, v24
	v_cvt_pk_bf16_f32 v91, v40, v26
	v_cvt_pk_bf16_f32 v96, v42, v28
	v_cvt_pk_bf16_f32 v97, v44, v30
	v_cvt_pk_bf16_f32 v98, v46, v32
	v_cvt_pk_bf16_f32 v99, v48, v36
	v_cvt_pk_bf16_f32 v104, v59, v21
	v_cvt_pk_bf16_f32 v105, v57, v25
	v_cvt_pk_bf16_f32 v106, v56, v27
	v_cvt_pk_bf16_f32 v107, v41, v29
	v_cvt_pk_bf16_f32 v112, v43, v31
	v_cvt_pk_bf16_f32 v113, v45, v33
	v_cvt_pk_bf16_f32 v114, v47, v37
	v_cvt_pk_bf16_f32 v115, v49, v39
	s_cmp_lt_i32 s47, s54
	s_cbranch_scc1 .LBB0_574
	s_branch .LBB0_573
; #define LAS __attribute__((address_space(3)))
; __device__ __forceinline__ int crow(int r, int hi) { return (r & 3) + 8 * (r >> 2) + 4 * hi; }
; __device__ __forceinline__ void qkt(f32x16& p0, f32x16& p1, const LAS unsigned char* Kb, const bf16x8 (&qr)[4], float cinit, int r32, int hi) {
;     const int sw = (r32 >> 1) & 7;
;     bf16x8 kf[8];
; #pragma unroll
;     for (int d0 = 0; d0 < 4; ++d0) {
;         unsigned ka = (unsigned)(uintptr_t)Kb + r32 * 128 + (((2 * d0 + hi) ^ sw) << 4); asm volatile("" : "+v"(ka));
;         kf[2 * d0] = *(const LAS bf16x8*)(uintptr_t)ka;
;         kf[2 * d0 + 1] = *(const LAS bf16x8*)(uintptr_t)(ka + 4096);
;     }
; #pragma unroll
;     for (int r = 0; r < 16; ++r) { p0[r] = cinit; p1[r] = cinit; }
;     __builtin_amdgcn_sched_barrier(0);
; #pragma unroll
;     for (int d0 = 0; d0 < 4; ++d0) {
;         p0 = __builtin_amdgcn_mfma_f32_32x32x16_bf16(kf[2 * d0], qr[d0], p0, 0, 0, 0);
;         p1 = __builtin_amdgcn_mfma_f32_32x32x16_bf16(kf[2 * d0 + 1], qr[d0], p1, 0, 0, 0);
;     }
; __device__ __forceinline__ void at_dil(const Args& a, LAS unsigned char* lds, int layer) {
;     ...
;             mt = other_half_max(mt);
;             m_run = mt;
; #pragma unroll
;             for (int j = 0; j < 3; ++j) {
;                 const int tt = twlo + 2 - j;
;                 if (tt >= tt_lo) {
;                     f32x16 p0, p1;
;                     qkt(p0, p1, lds + L_K + tt * 8192, qr, -mt, r32, hi);
;                     const LAS float* tb = tab + (32 * wid + r32 + 192 - 64 * tt - 4 * hi - 63);
; #pragma unroll
;                     for (int r = 0; r < 16; ++r) { p0[r] += tb[63 - crow(r, 0)]; p1[r] += tb[31 - crow(r, 0)]; }
;                     exp_sum(p0, p1, l_part);
;                     pw[j][0] = (u32x4){cvtpk(p0[0], p0[1]), cvtpk(p0[2], p0[3]), cvtpk(p0[4], p0[5]), cvtpk(p0[6], p0[7])};
;                     pw[j][1] = (u32x4){cvtpk(p0[8], p0[9]), cvtpk(p0[10], p0[11]), cvtpk(p0[12], p0[13]), cvtpk(p0[14], p0[15])};
;                     pw[j][2] = (u32x4){cvtpk(p1[0], p1[1]), cvtpk(p1[2], p1[3]), cvtpk(p1[4], p1[5]), cvtpk(p1[6], p1[7])};
;                     pw[j][3] = (u32x4){cvtpk(p1[8], p1[9]), cvtpk(p1[10], p1[11]), cvtpk(p1[12], p1[13]), cvtpk(p1[14], p1[15])};
.LBB0_565:
	v_mov_b32_e32 v18, v58
	s_nop 1
	v_permlane32_swap_b32_e32 v58, v18
	v_max_f32_e32 v18, v18, v18
	v_max_f32_e32 v19, v58, v58
	v_max_f32_e32 v137, v19, v18
	v_xor_b32_e32 v18, 0x80000000, v137
	v_mov_b32_e32 v19, v18
	v_mov_b32_e32 v20, v18
	v_mov_b32_e32 v21, v18
	v_mov_b32_e32 v22, v18
	v_mov_b32_e32 v23, v18
	v_mov_b32_e32 v24, v18
	v_mov_b32_e32 v25, v18
	v_mov_b32_e32 v26, v18
	v_mov_b32_e32 v27, v18
	v_mov_b32_e32 v28, v18
	v_mov_b32_e32 v29, v18
	v_mov_b32_e32 v30, v18
	v_mov_b32_e32 v31, v18
	v_mov_b32_e32 v32, v18
	v_mov_b32_e32 v33, v18
	s_cmp_ge_i32 s42, s54
	v_mov_b32_e32 v138, 0
	s_cbranch_scc0 .LBB0_589
	v_add_u32_e32 v36, s46, v143
	v_add_u32_e32 v37, v144, v36
	ds_read_b128 v[52:55], v37
	ds_read_b128 v[88:91], v37 offset:4096
	v_add_u32_e32 v37, v142, v36
	ds_read_b128 v[96:99], v37
	ds_read_b128 v[104:107], v37 offset:4096
	v_add_u32_e32 v37, v141, v36
	v_add_u32_e32 v36, v140, v36
	ds_read_b128 v[112:115], v37
	ds_read_b128 v[146:149], v37 offset:4096
	ds_read_b128 v[150:153], v36
	ds_read_b128 v[154:157], v36 offset:4096
	s_waitcnt lgkmcnt(7)
	v_mfma_f32_32x32x16_bf16 v[36:51], v[52:55], v[68:71], v[18:33]
	s_waitcnt lgkmcnt(6)
	v_mfma_f32_32x32x16_bf16 v[52:67], v[88:91], v[68:71], v[18:33]
	v_lshlrev_b32_e32 v88, 2, v139
	v_add_lshl_u32 v89, v136, s43, 2
	s_waitcnt lgkmcnt(5)
	v_mfma_f32_32x32x16_bf16 v[36:51], v[96:99], v[72:75], v[36:51]
	s_waitcnt lgkmcnt(4)
	v_mfma_f32_32x32x16_bf16 v[52:67], v[104:107], v[72:75], v[52:67]
	v_add3_u32 v104, s73, v88, v89
	s_waitcnt lgkmcnt(3)
	v_mfma_f32_32x32x16_bf16 v[36:51], v[112:115], v[76:79], v[36:51]
	ds_read2_b32 v[162:163], v104 offset0:191 offset1:192
	ds_read2_b32 v[164:165], v104 offset0:189 offset1:190
	ds_read2_b32 v[166:167], v104 offset0:159 offset1:160
	ds_read2_b32 v[168:169], v104 offset0:157 offset1:158
	s_waitcnt lgkmcnt(6)
	v_mfma_f32_32x32x16_bf16 v[52:67], v[146:149], v[76:79], v[52:67]
	ds_read2_b32 v[170:171], v104 offset0:183 offset1:184
	ds_read2_b32 v[172:173], v104 offset0:181 offset1:182
	ds_read2_b32 v[174:175], v104 offset0:151 offset1:152
	ds_read2_b32 v[176:177], v104 offset0:149 offset1:150
	s_waitcnt lgkmcnt(9)
	v_mfma_f32_32x32x16_bf16 v[36:51], v[150:153], v[80:83], v[36:51]
	ds_read2_b32 v[178:179], v104 offset0:175 offset1:176
	ds_read2_b32 v[180:181], v104 offset0:173 offset1:174
	ds_read2_b32 v[182:183], v104 offset0:143 offset1:144
	ds_read2_b32 v[184:185], v104 offset0:141 offset1:142
	s_waitcnt lgkmcnt(12)
	v_mfma_f32_32x32x16_bf16 v[52:67], v[154:157], v[80:83], v[52:67]
	ds_read2_b32 v[186:187], v104 offset0:167 offset1:168
	ds_read2_b32 v[188:189], v104 offset0:135 offset1:136
	s_waitcnt lgkmcnt(12)
	ds_read2_b32 v[190:191], v104 offset0:165 offset1:166
	ds_read2_b32 v[192:193], v104 offset0:133 offset1:134
	s_nop 11
	v_add_f32_e32 v89, v36, v163
	v_add_f32_e32 v88, v37, v162
	v_add_f32_e32 v91, v38, v165
	v_add_f32_e32 v90, v39, v164
	v_exp_f32_e32 v89, v89
	s_waitcnt lgkmcnt(13)
	v_add_f32_e32 v97, v52, v167
	v_add_f32_e32 v96, v53, v166
	s_waitcnt lgkmcnt(12)
	v_add_f32_e32 v99, v54, v169
	v_add_f32_e32 v98, v55, v168
	s_waitcnt lgkmcnt(11)
	v_add_f32_e32 v105, v40, v171
	s_waitcnt lgkmcnt(9)
	v_add_f32_e32 v53, v56, v175
	v_add_f32_e32 v56, v41, v170
	v_add_f32_e32 v52, v57, v174
	v_add_f32_e32 v57, v42, v173
	s_waitcnt lgkmcnt(8)
	v_add_f32_e32 v55, v58, v177
	v_add_f32_e32 v58, v43, v172
	v_add_f32_e32 v54, v59, v176
	s_waitcnt lgkmcnt(7)
	v_add_f32_e32 v59, v44, v179
	v_add_f32_e32 v106, v45, v178
	s_waitcnt lgkmcnt(5)
	v_add_f32_e32 v60, v60, v183
	v_add_f32_e32 v61, v61, v182
	v_add_f32_e32 v107, v46, v181
	v_add_f32_e32 v112, v47, v180
	v_exp_f32_e32 v145, v97
	s_waitcnt lgkmcnt(4)
	v_add_f32_e32 v62, v62, v185
	v_add_f32_e32 v63, v63, v184
	s_waitcnt lgkmcnt(3)
	v_add_f32_e32 v113, v48, v187
	s_waitcnt lgkmcnt(2)
	v_add_f32_e32 v64, v64, v189
	v_exp_f32_e32 v37, v88
	v_exp_f32_e32 v39, v96
	v_add_f32_e32 v104, v49, v186
	v_add_f32_e32 v65, v65, v188
	v_add_f32_e32 v36, v89, v145
	v_mov_b32_e32 v38, v35
	s_waitcnt lgkmcnt(1)
	v_add_f32_e32 v114, v50, v191
	v_add_f32_e32 v115, v51, v190
	v_exp_f32_e32 v91, v91
	v_exp_f32_e32 v146, v99
	v_pk_add_f32 v[40:41], v[36:37], v[38:39]
	v_exp_f32_e32 v36, v90
	s_waitcnt lgkmcnt(0)
	v_add_f32_e32 v66, v66, v43
	v_exp_f32_e32 v43, v98
	v_pk_add_f32 v[40:41], v[40:41], v[40:41] op_sel:[0,1] op_sel_hi:[1,0]
	v_add_f32_e32 v67, v67, v42
	v_add_f32_e32 v42, v91, v146
	v_mov_b32_e32 v41, v36
	v_exp_f32_e32 v38, v105
	v_exp_f32_e32 v147, v53
	v_pk_add_f32 v[40:41], v[40:41], v[42:43]
	v_exp_f32_e32 v42, v56
	v_exp_f32_e32 v45, v52
	v_pk_add_f32 v[40:41], v[40:41], v[40:41] op_sel:[0,1] op_sel_hi:[1,0]
	v_add_f32_e32 v44, v38, v147
	v_mov_b32_e32 v41, v42
	v_exp_f32_e32 v56, v57
	v_exp_f32_e32 v57, v55
	v_pk_add_f32 v[40:41], v[40:41], v[44:45]
	v_exp_f32_e32 v44, v58
	v_exp_f32_e32 v47, v54
	v_pk_add_f32 v[40:41], v[40:41], v[40:41] op_sel:[0,1] op_sel_hi:[1,0]
	v_add_f32_e32 v46, v56, v57
	v_mov_b32_e32 v41, v44
	v_exp_f32_e32 v58, v59
	v_exp_f32_e32 v59, v60
	v_pk_add_f32 v[40:41], v[40:41], v[46:47]
	v_exp_f32_e32 v46, v106
	v_exp_f32_e32 v49, v61
	v_pk_add_f32 v[40:41], v[40:41], v[40:41] op_sel:[0,1] op_sel_hi:[1,0]
	v_add_f32_e32 v48, v58, v59
	v_mov_b32_e32 v41, v46
	v_exp_f32_e32 v60, v107
	v_exp_f32_e32 v61, v62
	v_pk_add_f32 v[40:41], v[40:41], v[48:49]
	v_exp_f32_e32 v48, v112
	v_exp_f32_e32 v51, v63
	v_pk_add_f32 v[40:41], v[40:41], v[40:41] op_sel:[0,1] op_sel_hi:[1,0]
	v_add_f32_e32 v50, v60, v61
	v_mov_b32_e32 v41, v48
	v_exp_f32_e32 v62, v113
	v_exp_f32_e32 v63, v64
	v_pk_add_f32 v[40:41], v[40:41], v[50:51]
	v_exp_f32_e32 v50, v104
	v_exp_f32_e32 v53, v65
	v_pk_add_f32 v[40:41], v[40:41], v[40:41] op_sel:[0,1] op_sel_hi:[1,0]
	v_add_f32_e32 v52, v62, v63
	v_mov_b32_e32 v41, v50
	v_exp_f32_e32 v64, v114
	v_exp_f32_e32 v65, v66
	v_pk_add_f32 v[40:41], v[40:41], v[52:53]
	v_exp_f32_e32 v52, v115
	v_exp_f32_e32 v55, v67
	v_pk_add_f32 v[40:41], v[40:41], v[40:41] op_sel:[0,1] op_sel_hi:[1,0]
	v_add_f32_e32 v54, v64, v65
	v_mov_b32_e32 v41, v52
	v_pk_add_f32 v[40:41], v[40:41], v[54:55]
	v_cvt_pk_bf16_f32 v88, v89, v37
	v_add_f32_e32 v40, v40, v41
	v_add_f32_e32 v138, 0, v40
	v_cvt_pk_bf16_f32 v89, v91, v36
	v_cvt_pk_bf16_f32 v90, v38, v42
	v_cvt_pk_bf16_f32 v91, v56, v44
	v_cvt_pk_bf16_f32 v96, v58, v46
	v_cvt_pk_bf16_f32 v97, v60, v48
	v_cvt_pk_bf16_f32 v98, v62, v50
	v_cvt_pk_bf16_f32 v99, v64, v52
	v_cvt_pk_bf16_f32 v104, v145, v39
	v_cvt_pk_bf16_f32 v105, v146, v43
	v_cvt_pk_bf16_f32 v106, v147, v45
	v_cvt_pk_bf16_f32 v107, v57, v47
	v_cvt_pk_bf16_f32 v112, v59, v49
	v_cvt_pk_bf16_f32 v113, v61, v51
	v_cvt_pk_bf16_f32 v114, v63, v53
	v_cvt_pk_bf16_f32 v115, v65, v55
	s_cmp_lt_i32 s47, s54
	s_cbranch_scc0 .LBB0_590

; #define LAS __attribute__((address_space(3)))
; __device__ __forceinline__ int crow(int r, int hi) { return (r & 3) + 8 * (r >> 2) + 4 * hi; }
; __device__ __forceinline__ unsigned cvtpk(float lo, float hi) { f32x2_t v = {lo, hi}; bf16x2_t b = __builtin_convertvector(v, bf16x2_t); return __builtin_bit_cast(unsigned, b); }
; __device__ __forceinline__ void exp_sum(f32x16& p0, f32x16& p1, float& l_part) {
;     float rs = 0.f;
; #pragma unroll
;     for (int r = 0; r < 16; ++r) { p0[r] = __builtin_amdgcn_exp2f(p0[r]); p1[r] = __builtin_amdgcn_exp2f(p1[r]); rs += p0[r] + p1[r]; }
;     l_part += rs;
; __device__ __forceinline__ void at_dil(const Args& a, LAS unsigned char* lds, int layer) {
;     ...
;             for (int j = 0; j < 3; ++j) {
;                 const int tt = twlo + 2 - j;
;                 if (tt >= tt_lo) {
;                     f32x16 p0, p1;
;                     qkt(p0, p1, lds + L_K + tt * 8192, qr, -m_dil, r32, hi);
;                     const LAS float* tb = tab + (32 * wid + r32 + 192 - 64 * tt - 4 * hi - 63);
; #pragma unroll
;                     for (int r = 0; r < 16; ++r) { p0[r] += tb[63 - crow(r, 0)]; p1[r] += tb[31 - crow(r, 0)]; }
;                     exp_sum(p0, p1, l_part);
;                     pw[j][0] = (u32x4){cvtpk(p0[0], p0[1]), cvtpk(p0[2], p0[3]), cvtpk(p0[4], p0[5]), cvtpk(p0[6], p0[7])};
;                     pw[j][1] = (u32x4){cvtpk(p0[8], p0[9]), cvtpk(p0[10], p0[11]), cvtpk(p0[12], p0[13]), cvtpk(p0[14], p0[15])};
;                     pw[j][2] = (u32x4){cvtpk(p1[0], p1[1]), cvtpk(p1[2], p1[3]), cvtpk(p1[4], p1[5]), cvtpk(p1[6], p1[7])};
;                     pw[j][3] = (u32x4){cvtpk(p1[8], p1[9]), cvtpk(p1[10], p1[11]), cvtpk(p1[12], p1[13]), cvtpk(p1[14], p1[15])};
.LBB0_573:
	s_nop 2
	v_add_u32_e32 v18, s48, v143
	v_add_u32_e32 v19, v144, v18
	ds_read_b128 v[36:39], v19
	ds_read_b128 v[54:57], v19 offset:4096
	v_add_u32_e32 v19, v142, v18
	ds_read_b128 v[58:61], v19
	ds_read_b128 v[62:65], v19 offset:4096
	v_add_u32_e32 v19, v141, v18
	v_add_u32_e32 v18, v140, v18
	ds_read_b128 v[84:87], v19
	ds_read_b128 v[92:95], v19 offset:4096
	ds_read_b128 v[100:103], v18
	ds_read_b128 v[108:111], v18 offset:4096
	s_waitcnt lgkmcnt(7)
	v_mfma_f32_32x32x16_bf16 v[18:33], v[36:39], v[68:71], v[2:17]
	v_add_lshl_u32 v53, v136, s43, 2
	s_waitcnt lgkmcnt(6)
	v_mfma_f32_32x32x16_bf16 v[36:51], v[54:57], v[68:71], v[2:17]
	s_waitcnt lgkmcnt(5)
	v_mfma_f32_32x32x16_bf16 v[18:33], v[58:61], v[72:75], v[18:33]
	v_add3_u32 v60, s75, v52, v53
	s_waitcnt lgkmcnt(4)
	v_mfma_f32_32x32x16_bf16 v[36:51], v[62:65], v[72:75], v[36:51]
	ds_read2_b32 v[162:163], v60 offset0:191 offset1:192
	ds_read2_b32 v[164:165], v60 offset0:189 offset1:190
	ds_read2_b32 v[166:167], v60 offset0:159 offset1:160
	ds_read2_b32 v[168:169], v60 offset0:157 offset1:158
	s_waitcnt lgkmcnt(7)
	v_mfma_f32_32x32x16_bf16 v[18:33], v[84:87], v[76:79], v[18:33]
	ds_read2_b32 v[170:171], v60 offset0:183 offset1:184
	ds_read2_b32 v[172:173], v60 offset0:181 offset1:182
	ds_read2_b32 v[174:175], v60 offset0:151 offset1:152
	ds_read2_b32 v[176:177], v60 offset0:149 offset1:150
	s_waitcnt lgkmcnt(10)
	v_mfma_f32_32x32x16_bf16 v[36:51], v[92:95], v[76:79], v[36:51]
	ds_read2_b32 v[178:179], v60 offset0:175 offset1:176
	ds_read2_b32 v[180:181], v60 offset0:173 offset1:174
	ds_read2_b32 v[182:183], v60 offset0:143 offset1:144
	ds_read2_b32 v[184:185], v60 offset0:141 offset1:142
	s_waitcnt lgkmcnt(13)
	v_mfma_f32_32x32x16_bf16 v[18:33], v[100:103], v[80:83], v[18:33]
	ds_read2_b32 v[186:187], v60 offset0:167 offset1:168
	s_waitcnt lgkmcnt(12)
	ds_read2_b32 v[188:189], v60 offset0:135 offset1:136
	v_mfma_f32_32x32x16_bf16 v[36:51], v[108:111], v[80:83], v[36:51]
	ds_read2_b32 v[190:191], v60 offset0:165 offset1:166
	s_waitcnt lgkmcnt(12)
	ds_read2_b32 v[192:193], v60 offset0:133 offset1:134
	s_nop 11
	v_add_f32_e32 v53, v18, v163
	v_add_f32_e32 v52, v19, v162
	v_add_f32_e32 v55, v20, v165
	v_add_f32_e32 v54, v21, v164
	v_exp_f32_e32 v53, v53
	v_add_f32_e32 v57, v36, v167
	v_add_f32_e32 v56, v37, v166
	s_waitcnt lgkmcnt(12)
	v_add_f32_e32 v59, v38, v169
	v_add_f32_e32 v58, v39, v168
	s_waitcnt lgkmcnt(11)
	v_add_f32_e32 v61, v22, v171
	s_waitcnt lgkmcnt(9)
	v_add_f32_e32 v37, v40, v175
	v_add_f32_e32 v40, v23, v170
	v_add_f32_e32 v36, v41, v174
	v_add_f32_e32 v41, v24, v173
	s_waitcnt lgkmcnt(8)
	v_add_f32_e32 v39, v42, v177
	v_add_f32_e32 v42, v25, v172
	v_add_f32_e32 v38, v43, v176
	s_waitcnt lgkmcnt(7)
	v_add_f32_e32 v43, v26, v179
	v_add_f32_e32 v62, v27, v178
	s_waitcnt lgkmcnt(5)
	v_add_f32_e32 v44, v44, v183
	v_add_f32_e32 v45, v45, v182
	v_add_f32_e32 v63, v28, v181
	v_add_f32_e32 v64, v29, v180
	v_exp_f32_e32 v57, v57
	s_waitcnt lgkmcnt(4)
	v_add_f32_e32 v46, v46, v185
	v_add_f32_e32 v47, v47, v184
	s_waitcnt lgkmcnt(3)
	v_add_f32_e32 v65, v30, v187
	s_waitcnt lgkmcnt(2)
	v_add_f32_e32 v48, v48, v189
	v_exp_f32_e32 v19, v52
	v_exp_f32_e32 v21, v56
	v_add_f32_e32 v60, v31, v186
	v_add_f32_e32 v49, v49, v188
	v_add_f32_e32 v18, v53, v57
	v_mov_b32_e32 v20, v35
	s_waitcnt lgkmcnt(1)
	v_add_f32_e32 v66, v32, v191
	v_add_f32_e32 v67, v33, v190
	v_exp_f32_e32 v52, v55
	v_exp_f32_e32 v55, v59
	v_pk_add_f32 v[22:23], v[18:19], v[20:21]
	v_exp_f32_e32 v18, v54
	s_waitcnt lgkmcnt(0)
	v_add_f32_e32 v50, v50, v25
	v_exp_f32_e32 v25, v58
	v_pk_add_f32 v[22:23], v[22:23], v[22:23] op_sel:[0,1] op_sel_hi:[1,0]
	v_add_f32_e32 v51, v51, v24
	v_add_f32_e32 v24, v52, v55
	v_mov_b32_e32 v23, v18
	v_exp_f32_e32 v20, v61
	v_exp_f32_e32 v54, v37
	v_pk_add_f32 v[22:23], v[22:23], v[24:25]
	v_exp_f32_e32 v24, v40
	v_exp_f32_e32 v27, v36
	v_pk_add_f32 v[22:23], v[22:23], v[22:23] op_sel:[0,1] op_sel_hi:[1,0]
	v_add_f32_e32 v26, v20, v54
	v_mov_b32_e32 v23, v24
	v_exp_f32_e32 v40, v41
	v_exp_f32_e32 v41, v39
	v_pk_add_f32 v[22:23], v[22:23], v[26:27]
	v_exp_f32_e32 v26, v42
	v_exp_f32_e32 v29, v38
	v_pk_add_f32 v[22:23], v[22:23], v[22:23] op_sel:[0,1] op_sel_hi:[1,0]
	v_add_f32_e32 v28, v40, v41
	v_mov_b32_e32 v23, v26
	v_exp_f32_e32 v42, v43
	v_exp_f32_e32 v43, v44
	v_pk_add_f32 v[22:23], v[22:23], v[28:29]
	v_exp_f32_e32 v28, v62
	v_exp_f32_e32 v31, v45
	v_pk_add_f32 v[22:23], v[22:23], v[22:23] op_sel:[0,1] op_sel_hi:[1,0]
	v_add_f32_e32 v30, v42, v43
	v_mov_b32_e32 v23, v28
	v_exp_f32_e32 v44, v63
	v_exp_f32_e32 v45, v46
	v_pk_add_f32 v[22:23], v[22:23], v[30:31]
	v_exp_f32_e32 v30, v64
	v_exp_f32_e32 v33, v47
	v_pk_add_f32 v[22:23], v[22:23], v[22:23] op_sel:[0,1] op_sel_hi:[1,0]
	v_add_f32_e32 v32, v44, v45
	v_mov_b32_e32 v23, v30
	v_exp_f32_e32 v46, v65
	v_exp_f32_e32 v47, v48
	v_pk_add_f32 v[22:23], v[22:23], v[32:33]
	v_exp_f32_e32 v32, v60
	v_exp_f32_e32 v37, v49
	v_pk_add_f32 v[22:23], v[22:23], v[22:23] op_sel:[0,1] op_sel_hi:[1,0]
	v_add_f32_e32 v36, v46, v47
	v_mov_b32_e32 v23, v32
	v_exp_f32_e32 v48, v66
	v_exp_f32_e32 v49, v50
	v_pk_add_f32 v[22:23], v[22:23], v[36:37]
	v_exp_f32_e32 v36, v67
	v_exp_f32_e32 v39, v51
	v_pk_add_f32 v[22:23], v[22:23], v[22:23] op_sel:[0,1] op_sel_hi:[1,0]
	v_add_f32_e32 v38, v48, v49
	v_mov_b32_e32 v23, v36
	v_pk_add_f32 v[22:23], v[22:23], v[38:39]
	v_cvt_pk_bf16_f32 v84, v53, v19
	v_add_f32_e32 v22, v22, v23
	v_add_f32_e32 v138, v138, v22
	v_cvt_pk_bf16_f32 v85, v52, v18
	v_cvt_pk_bf16_f32 v86, v20, v24
	v_cvt_pk_bf16_f32 v87, v40, v26
	v_cvt_pk_bf16_f32 v92, v42, v28
	v_cvt_pk_bf16_f32 v93, v44, v30
	v_cvt_pk_bf16_f32 v94, v46, v32
	v_cvt_pk_bf16_f32 v95, v48, v36
	v_cvt_pk_bf16_f32 v100, v57, v21
	v_cvt_pk_bf16_f32 v101, v55, v25
	v_cvt_pk_bf16_f32 v102, v54, v27
	v_cvt_pk_bf16_f32 v103, v41, v29
	v_cvt_pk_bf16_f32 v108, v43, v31
	v_cvt_pk_bf16_f32 v109, v45, v33
	v_cvt_pk_bf16_f32 v110, v47, v37
	v_cvt_pk_bf16_f32 v111, v49, v39
